# first grid barrier: after the census it now uses the same single-level arrival/release protocol with early L1 invalidate as barriers 2..13 (original XSUB/TOP/TOPGEN/XGEN code removed)
# speedup vs baseline: 1.0054x; 1.0042x over previous
; __device__ __forceinline__ unsigned xb_ld(unsigned* p)              { return __hip_atomic_load(p, __ATOMIC_RELAXED, __HIP_MEMORY_SCOPE_AGENT); }
; __device__ __forceinline__ unsigned xb_add(unsigned* p, unsigned v) { return __hip_atomic_fetch_add(p, v, __ATOMIC_RELAXED, __HIP_MEMORY_SCOPE_AGENT); }
; #define XB_SPIN(cond, bar) do { unsigned _sp = 0; while (cond) { __builtin_amdgcn_s_sleep(1); \
;     if ((++_sp & 255u) == 0u) { if (xb_ld(&(bar)[XB_TMO])) break; if (_sp > XB_SPIN_CAP) { atomicAdd(&(bar)[XB_TMO], 1u); break; } } } } while (0)
; __device__ __forceinline__ void xcd_barrier(const XcdBarrier& b) {
;   asm volatile("s_waitcnt vmcnt(0)" ::: "memory");
;   __syncthreads();
;   if (threadIdx.x == 0) {
;     unsigned* bar = b.bar;
;     __builtin_amdgcn_s_waitcnt(0);
;     unsigned nloc = b.st[0], nx = b.st[1];
;     if (nloc == 0u) { xcd_barrier_complete(bar, b.x, nloc, nx); b.st[0] = nloc; b.st[1] = nx; }
;     const unsigned old = xb_add(&bar[XB_XSUB(b.x)], 1u);
;     const unsigned gen = old / nloc;
;     if (old + 1u == (gen + 1u) * nloc) {
;       __builtin_amdgcn_fence(__ATOMIC_RELEASE, "agent");
;       asm volatile("s_waitcnt vmcnt(0)" ::: "memory");
;       const unsigned og = xb_add(&bar[XB_TOP], 1u);
;       const unsigned tg = og / nx;
;       if (og + 1u == (tg + 1u) * nx) xb_add(&bar[XB_TOPGEN], 1u);
;       else XB_SPIN(xb_ld(&bar[XB_TOPGEN]) == tg, bar);
;       __builtin_amdgcn_fence(__ATOMIC_ACQUIRE, "agent");
;       xb_add(&bar[XB_XGEN(b.x)], 1u);
;       asm volatile("s_waitcnt vmcnt(0)" ::: "memory");
;     } else {
;       XB_SPIN(xb_ld(&bar[XB_XGEN(b.x)]) == gen, bar);
;       __builtin_amdgcn_fence(__ATOMIC_ACQUIRE, "agent");
;       asm volatile("s_waitcnt vmcnt(0)" ::: "memory");
;     }
;   }
;   __syncthreads();
; }
.LBB0_72:
	s_waitcnt vmcnt(0) lgkmcnt(0)
	s_add_u32 s98, s98, 1
	v_mov_b32_e32 v253, 0x12810
	ds_read_b32 v254, v253
	ds_read_b32 v253, v253 offset:4
	s_lshl_b32 s101, s33, 8
	s_add_u32 s99, s101, 5120
	s_waitcnt lgkmcnt(0)
	v_readfirstlane_b32 s100, v254
	v_mov_b32_e32 v254, s99
	v_readfirstlane_b32 s99, v253
	s_nop 0
	v_mov_b32_e32 v253, v254
	v_mov_b32_e32 v254, 1
	global_atomic_add v254, v253, v254, s[44:45] offset:64 sc0
	buffer_inv sc1
	s_mul_i32 s100, s100, s98
	s_mul_i32 s99, s99, s98
	s_waitcnt vmcnt(0)
	v_add_u32_e32 v254, 1, v254
	v_cmp_ne_u32_e32 vcc, s100, v254
	s_cbranch_vccnz .Lgb_wait_1
	buffer_wbl2 sc1
	s_waitcnt vmcnt(0)
	v_mov_b32_e32 v254, 1
	v_mov_b32_e32 v253, 9216
	global_atomic_add v253, v254, s[44:45] offset:64
	global_atomic_add v253, v254, s[44:45] offset:320
	global_atomic_add v253, v254, s[44:45] offset:576
	global_atomic_add v253, v254, s[44:45] offset:832
	global_atomic_add v253, v254, s[44:45] offset:1088
	global_atomic_add v253, v254, s[44:45] offset:1344
	global_atomic_add v253, v254, s[44:45] offset:1600
	global_atomic_add v253, v254, s[44:45] offset:1856
	v_mov_b32_e32 v253, 11264
	global_atomic_add v253, v254, s[44:45] offset:64
	global_atomic_add v253, v254, s[44:45] offset:320
	global_atomic_add v253, v254, s[44:45] offset:576
	global_atomic_add v253, v254, s[44:45] offset:832
	global_atomic_add v253, v254, s[44:45] offset:1088
	global_atomic_add v253, v254, s[44:45] offset:1344
	global_atomic_add v253, v254, s[44:45] offset:1600
	global_atomic_add v253, v254, s[44:45] offset:1856

; __device__ __forceinline__ unsigned xb_ld(unsigned* p)              { return __hip_atomic_load(p, __ATOMIC_RELAXED, __HIP_MEMORY_SCOPE_AGENT); }
; __device__ __forceinline__ unsigned xb_add(unsigned* p, unsigned v) { return __hip_atomic_fetch_add(p, v, __ATOMIC_RELAXED, __HIP_MEMORY_SCOPE_AGENT); }
; #define XB_SPIN(cond, bar) do { unsigned _sp = 0; while (cond) { __builtin_amdgcn_s_sleep(1); \
;     if ((++_sp & 255u) == 0u) { if (xb_ld(&(bar)[XB_TMO])) break; if (_sp > XB_SPIN_CAP) { atomicAdd(&(bar)[XB_TMO], 1u); break; } } } } while (0)
; __device__ void phase_fold(KParams& p, int bid, int nb, char* smem) {
;     ...
;   for (int i = bid * NTHREADS + tid; i < 5 * NMOD; i += nb * NTHREADS) {
;     int col = i % NMOD;
;     float s = p.b_mod[col];
;     for (int ks = 0; ks < KSPLIT; ++ks) s += p.partial[(size_t)ks * 5 * NMOD + i];
;     p.mod[i] = s;
;   }
; __device__ __forceinline__ void xcd_barrier(const XcdBarrier& b) {
;     ...
;     const unsigned old = xb_add(&bar[XB_XSUB(b.x)], 1u);
;     const unsigned gen = old / nloc;
;     if (old + 1u == (gen + 1u) * nloc) {
;       __builtin_amdgcn_fence(__ATOMIC_RELEASE, "agent");
;       asm volatile("s_waitcnt vmcnt(0)" ::: "memory");
;       const unsigned og = xb_add(&bar[XB_TOP], 1u);
;       const unsigned tg = og / nx;
;       if (og + 1u == (tg + 1u) * nx) xb_add(&bar[XB_TOPGEN], 1u);
;       else XB_SPIN(xb_ld(&bar[XB_TOPGEN]) == tg, bar);
;       __builtin_amdgcn_fence(__ATOMIC_ACQUIRE, "agent");
;       xb_add(&bar[XB_XGEN(b.x)], 1u);
;       asm volatile("s_waitcnt vmcnt(0)" ::: "memory");
;     } else {
;       XB_SPIN(xb_ld(&bar[XB_XGEN(b.x)]) == gen, bar);
;       __builtin_amdgcn_fence(__ATOMIC_ACQUIRE, "agent");
;       asm volatile("s_waitcnt vmcnt(0)" ::: "memory");
;     }
.Lgb_wd_1:
.LBB0_108:
	s_or_b64 exec, exec, s[6:7]
	v_lshl_or_b32 v134, s2, 8, v0
	s_mov_b32 s3, 0xf000
	s_mov_b64 s[12:13], s[0:1]
	v_cmp_gt_i32_e32 vcc, s3, v134
	s_waitcnt lgkmcnt(0)
	s_barrier
	s_and_saveexec_b64 s[6:7], vcc
	s_cbranch_execz .LBB0_111
	s_load_dwordx2 s[14:15], s[12:13], 0x28
	s_load_dwordx4 s[8:11], s[12:13], 0x180
	s_lshl_b32 s16, s34, 8
	v_ashrrev_i32_e32 v135, 31, v134
	s_ashr_i32 s17, s16, 31
	v_lshlrev_b64 v[2:3], 2, v[134:135]
	s_lshl_b64 s[18:19], s[16:17], 2
	s_mov_b64 s[20:21], 0
	s_mov_b32 s3, 0x2aaaaaab
	s_mov_b32 s17, 0x3c000
	s_mov_b32 s22, 0x78000
	s_mov_b32 s23, 0xb4000
	s_mov_b32 s24, 0xf0000
	s_mov_b32 s25, 0x12c000
	s_mov_b32 s26, 0x168000
	s_mov_b32 s27, 0x1a4000
	s_mov_b32 s28, 0x1e0000
	s_mov_b32 s29, 0x21c000
	s_mov_b32 s30, 0x258000
	s_mov_b32 s31, 0x294000
	s_mov_b32 s35, 0x2d0000
	s_mov_b32 s36, 0x30c000
	s_mov_b32 s37, 0x348000
	s_mov_b32 s38, 0x384000
	s_mov_b32 s39, 0x3c0000
	s_mov_b32 s40, 0x3fc000
	s_mov_b32 s41, 0x438000
	s_mov_b32 s42, 0x474000
	s_mov_b32 s43, 0x4b0000
	s_mov_b32 s46, 0x4ec000
	s_mov_b32 s47, 0x528000
	s_mov_b32 s48, 0x564000
	s_mov_b32 s49, 0x5a0000
	s_mov_b32 s50, 0x5dc000
	s_mov_b32 s51, 0x618000
	s_mov_b32 s52, 0x654000
	s_mov_b32 s53, 0x690000
	s_mov_b32 s54, 0x6cc000
	s_mov_b32 s55, 0x708000
	s_mov_b32 s56, 0x744000
	s_mov_b32 s57, 0xefff
	v_mov_b32_e32 v1, v134
